# speedup vs baseline: 1.0091x; 1.0091x over previous
.LBB2_25:
	s_sub_i32 s60, s6, s7
	s_cmp_lt_i32 s60, 4
	s_cbranch_scc1 .Lmy_part
	ds_read_b128 v[120:123], v118
	ds_read_b128 v[124:127], v118 offset:32
	ds_read2_b32 v[6:7], v118 offset0:36 offset1:44
	s_add_i32 s7, s7, 4
	s_cmp_ge_i32 s7, s6
	s_waitcnt vmcnt(3) lgkmcnt(2)
	v_pk_fma_f16 v109, v14, v120, v109
	v_pk_fma_f16 v97, v14, v121, v97
	v_pk_fma_f16 v90, v14, v122, v90
	v_pk_fma_f16 v85, v14, v123, v85
	v_pk_fma_f16 v108, v15, v120, v108
	v_pk_fma_f16 v95, v15, v121, v95
	v_pk_fma_f16 v89, v15, v122, v89
	v_pk_fma_f16 v84, v15, v123, v84
	v_pk_fma_f16 v107, v16, v120, v107
	v_pk_fma_f16 v94, v16, v121, v94
	v_pk_fma_f16 v88, v16, v122, v88
	v_pk_fma_f16 v82, v16, v123, v82
	v_pk_fma_f16 v105, v17, v120, v105
	v_pk_fma_f16 v92, v17, v121, v92
	v_pk_fma_f16 v87, v17, v122, v87
	v_pk_fma_f16 v81, v17, v123, v81
	s_waitcnt lgkmcnt(0)
	v_lshl_or_b32 v14, v6, 8, v72
	global_load_dwordx4 v[14:17], v14, s[16:17]
	ds_read_b128 v[120:123], v118 offset:64
	s_waitcnt vmcnt(3)
	v_pk_fma_f16 v109, v10, v124, v109
	v_pk_fma_f16 v97, v10, v125, v97
	v_pk_fma_f16 v90, v10, v126, v90
	v_pk_fma_f16 v85, v10, v127, v85
	v_pk_fma_f16 v108, v11, v124, v108
	v_pk_fma_f16 v95, v11, v125, v95
	v_pk_fma_f16 v89, v11, v126, v89
	v_pk_fma_f16 v84, v11, v127, v84
	v_pk_fma_f16 v107, v12, v124, v107
	v_pk_fma_f16 v94, v12, v125, v94
	v_pk_fma_f16 v88, v12, v126, v88
	v_pk_fma_f16 v82, v12, v127, v82
	v_pk_fma_f16 v105, v13, v124, v105
	v_pk_fma_f16 v92, v13, v125, v92
	v_pk_fma_f16 v87, v13, v126, v87
	v_pk_fma_f16 v81, v13, v127, v81
	v_lshl_or_b32 v10, v7, 8, v72
	global_load_dwordx4 v[10:13], v10, s[16:17]
	ds_read2_b32 v[8:9], v118 offset0:52 offset1:60
	ds_read_b128 v[124:127], v118 offset:96
	s_waitcnt vmcnt(3) lgkmcnt(2)
	v_pk_fma_f16 v109, v54, v120, v109
	v_pk_fma_f16 v97, v54, v121, v97
	v_pk_fma_f16 v90, v54, v122, v90
	v_pk_fma_f16 v85, v54, v123, v85
	v_pk_fma_f16 v108, v55, v120, v108
	v_pk_fma_f16 v95, v55, v121, v95
	v_pk_fma_f16 v89, v55, v122, v89
	v_pk_fma_f16 v84, v55, v123, v84
	v_pk_fma_f16 v107, v56, v120, v107
	v_pk_fma_f16 v94, v56, v121, v94
	v_pk_fma_f16 v88, v56, v122, v88
	v_pk_fma_f16 v82, v56, v123, v82
	v_pk_fma_f16 v105, v57, v120, v105
	v_pk_fma_f16 v92, v57, v121, v92
	v_pk_fma_f16 v87, v57, v122, v87
	v_pk_fma_f16 v81, v57, v123, v81
	s_waitcnt lgkmcnt(1)
	v_lshl_or_b32 v54, v8, 8, v72
	global_load_dwordx4 v[54:57], v54, s[16:17]
	v_add_u32_e32 v118, 0x80, v118
	s_waitcnt vmcnt(3) lgkmcnt(0)
	v_pk_fma_f16 v109, v58, v124, v109
	v_pk_fma_f16 v97, v58, v125, v97
	v_pk_fma_f16 v90, v58, v126, v90
	v_pk_fma_f16 v85, v58, v127, v85
	v_pk_fma_f16 v108, v59, v124, v108
	v_pk_fma_f16 v95, v59, v125, v95
	v_pk_fma_f16 v89, v59, v126, v89
	v_pk_fma_f16 v84, v59, v127, v84
	v_pk_fma_f16 v107, v60, v124, v107
	v_pk_fma_f16 v94, v60, v125, v94
	v_pk_fma_f16 v88, v60, v126, v88
	v_pk_fma_f16 v82, v60, v127, v82
	v_pk_fma_f16 v105, v61, v124, v105
	v_pk_fma_f16 v92, v61, v125, v92
	v_pk_fma_f16 v87, v61, v126, v87
	v_pk_fma_f16 v81, v61, v127, v81
	v_lshl_or_b32 v58, v9, 8, v72
	global_load_dwordx4 v[58:61], v58, s[16:17]
	s_cbranch_scc0 .LBB2_25
	s_branch .LBB2_26
.Lmy_part:
	ds_read_b128 v[120:123], v118
	s_waitcnt vmcnt(3) lgkmcnt(0)
	v_pk_fma_f16 v109, v14, v120, v109
	v_pk_fma_f16 v97, v14, v121, v97
	v_pk_fma_f16 v90, v14, v122, v90
	v_pk_fma_f16 v85, v14, v123, v85
	v_pk_fma_f16 v108, v15, v120, v108
	v_pk_fma_f16 v95, v15, v121, v95
	v_pk_fma_f16 v89, v15, v122, v89
	v_pk_fma_f16 v84, v15, v123, v84
	v_pk_fma_f16 v107, v16, v120, v107
	v_pk_fma_f16 v94, v16, v121, v94
	v_pk_fma_f16 v88, v16, v122, v88
	v_pk_fma_f16 v82, v16, v123, v82
	v_pk_fma_f16 v105, v17, v120, v105
	v_pk_fma_f16 v92, v17, v121, v92
	v_pk_fma_f16 v87, v17, v122, v87
	v_pk_fma_f16 v81, v17, v123, v81
	s_cmp_lt_i32 s60, 2
	s_cbranch_scc1 .LBB2_26
	ds_read_b128 v[124:127], v118 offset:32
	s_waitcnt vmcnt(2) lgkmcnt(0)
	v_pk_fma_f16 v109, v10, v124, v109
	v_pk_fma_f16 v97, v10, v125, v97
	v_pk_fma_f16 v90, v10, v126, v90
	v_pk_fma_f16 v85, v10, v127, v85
	v_pk_fma_f16 v108, v11, v124, v108
	v_pk_fma_f16 v95, v11, v125, v95
	v_pk_fma_f16 v89, v11, v126, v89
	v_pk_fma_f16 v84, v11, v127, v84
	v_pk_fma_f16 v107, v12, v124, v107
	v_pk_fma_f16 v94, v12, v125, v94
	v_pk_fma_f16 v88, v12, v126, v88
	v_pk_fma_f16 v82, v12, v127, v82
	v_pk_fma_f16 v105, v13, v124, v105
	v_pk_fma_f16 v92, v13, v125, v92
	v_pk_fma_f16 v87, v13, v126, v87
	v_pk_fma_f16 v81, v13, v127, v81
	s_cmp_lt_i32 s60, 3
	s_cbranch_scc1 .LBB2_26
	ds_read_b128 v[120:123], v118 offset:64
	s_waitcnt vmcnt(1) lgkmcnt(0)
	v_pk_fma_f16 v109, v54, v120, v109
	v_pk_fma_f16 v97, v54, v121, v97
	v_pk_fma_f16 v90, v54, v122, v90
	v_pk_fma_f16 v85, v54, v123, v85
	v_pk_fma_f16 v108, v55, v120, v108
	v_pk_fma_f16 v95, v55, v121, v95
	v_pk_fma_f16 v89, v55, v122, v89
	v_pk_fma_f16 v84, v55, v123, v84
	v_pk_fma_f16 v107, v56, v120, v107
	v_pk_fma_f16 v94, v56, v121, v94
	v_pk_fma_f16 v88, v56, v122, v88
	v_pk_fma_f16 v82, v56, v123, v82
	v_pk_fma_f16 v105, v57, v120, v105
	v_pk_fma_f16 v92, v57, v121, v92
	v_pk_fma_f16 v87, v57, v122, v87
	v_pk_fma_f16 v81, v57, v123, v81
